# scatter phases: 32 histogram loads per wave issued back to back instead of 15 serialized waits
# speedup vs baseline: 1.0042x; 1.0042x over previous
; __device__ __forceinline__ void phase_scatter(const Frame& F, int layer) {
;     ...
;     for (int vb = F.bid; vb < 256; vb += F.G) {
;         int all = 0, lo = 0;
;         for (int b = F.wave * 32; b < F.wave * 32 + 32; ++b) { const int h = HIST[b * 64 + F.lane]; all += h; lo += (b < vb) ? h : 0; }
;         pall[F.wave * 64 + F.lane] = all; plo[F.wave * 64 + F.lane] = lo;
;         const int rb = tok0 + vb * TPB;
;         for (int i = F.tid; i < TPB * 8; i += NTHREADS) sel_l[i] = SE[rb * 8 + i];
.LBB0_1394:
	global_load_dword v120, v[6:7], off
	global_load_dword v121, v[8:9], off
	global_load_dword v122, v[10:11], off
	global_load_dword v123, v[12:13], off
	global_load_dword v124, v[14:15], off
	global_load_dword v125, v[16:17], off
	global_load_dword v126, v[18:19], off
	global_load_dword v127, v[20:21], off
	global_load_dword v128, v[22:23], off
	global_load_dword v129, v[24:25], off
	global_load_dword v130, v[26:27], off
	global_load_dword v131, v[28:29], off
	global_load_dword v132, v[30:31], off
	global_load_dword v133, v[32:33], off
	global_load_dword v134, v[34:35], off
	global_load_dword v135, v[36:37], off
	global_load_dword v136, v[38:39], off
	global_load_dword v137, v[40:41], off
	global_load_dword v138, v[42:43], off
	global_load_dword v139, v[44:45], off
	global_load_dword v140, v[46:47], off
	global_load_dword v141, v[48:49], off
	global_load_dword v142, v[50:51], off
	global_load_dword v143, v[52:53], off
	global_load_dword v144, v[54:55], off
	global_load_dword v145, v[56:57], off
	global_load_dword v146, v[58:59], off
	global_load_dword v147, v[60:61], off
	global_load_dword v148, v[62:63], off
	global_load_dword v149, v[64:65], off
	global_load_dword v150, v[66:67], off
	global_load_dword v151, v[68:69], off
	s_sub_i32 s99, s2, s76
	v_mov_b32_e32 v72, 0
	s_waitcnt vmcnt(0)
	v_add_u32_e32 v3, v120, v121
	v_add3_u32 v3, v3, v122, v123
	v_add3_u32 v3, v3, v124, v125
	v_add3_u32 v3, v3, v126, v127
	v_add3_u32 v3, v3, v128, v129
	v_add3_u32 v3, v3, v130, v131
	v_add3_u32 v3, v3, v132, v133
	v_add3_u32 v3, v3, v134, v135
	v_add3_u32 v3, v3, v136, v137
	v_add3_u32 v3, v3, v138, v139
	v_add3_u32 v3, v3, v140, v141
	v_add3_u32 v3, v3, v142, v143
	v_add3_u32 v3, v3, v144, v145
	v_add3_u32 v3, v3, v146, v147
	v_add3_u32 v3, v3, v148, v149
	v_add3_u32 v3, v3, v150, v151
	s_cmp_gt_i32 s99, 0
	s_cselect_b64 vcc, -1, 0
	v_cndmask_b32_e32 v73, 0, v120, vcc
	v_add_u32_e32 v72, v72, v73
	s_cmp_gt_i32 s99, 1
	s_cselect_b64 vcc, -1, 0
	v_cndmask_b32_e32 v73, 0, v121, vcc
	v_add_u32_e32 v72, v72, v73
	s_cmp_gt_i32 s99, 2
	s_cselect_b64 vcc, -1, 0
	v_cndmask_b32_e32 v73, 0, v122, vcc
	v_add_u32_e32 v72, v72, v73
	s_cmp_gt_i32 s99, 3
	s_cselect_b64 vcc, -1, 0
	v_cndmask_b32_e32 v73, 0, v123, vcc
	v_add_u32_e32 v72, v72, v73
	s_cmp_gt_i32 s99, 4
	s_cselect_b64 vcc, -1, 0
	v_cndmask_b32_e32 v73, 0, v124, vcc
	v_add_u32_e32 v72, v72, v73
	s_cmp_gt_i32 s99, 5
	s_cselect_b64 vcc, -1, 0
	v_cndmask_b32_e32 v73, 0, v125, vcc
	v_add_u32_e32 v72, v72, v73
	s_cmp_gt_i32 s99, 6
	s_cselect_b64 vcc, -1, 0
	v_cndmask_b32_e32 v73, 0, v126, vcc
	v_add_u32_e32 v72, v72, v73
	s_cmp_gt_i32 s99, 7
	s_cselect_b64 vcc, -1, 0
	v_cndmask_b32_e32 v73, 0, v127, vcc
	v_add_u32_e32 v72, v72, v73
	s_cmp_gt_i32 s99, 8
	s_cselect_b64 vcc, -1, 0
	v_cndmask_b32_e32 v73, 0, v128, vcc
	v_add_u32_e32 v72, v72, v73
	s_cmp_gt_i32 s99, 9
	s_cselect_b64 vcc, -1, 0
	v_cndmask_b32_e32 v73, 0, v129, vcc
	v_add_u32_e32 v72, v72, v73
	s_cmp_gt_i32 s99, 10
	s_cselect_b64 vcc, -1, 0
	v_cndmask_b32_e32 v73, 0, v130, vcc
	v_add_u32_e32 v72, v72, v73
	s_cmp_gt_i32 s99, 11
	s_cselect_b64 vcc, -1, 0
	v_cndmask_b32_e32 v73, 0, v131, vcc
	v_add_u32_e32 v72, v72, v73
	s_cmp_gt_i32 s99, 12
	s_cselect_b64 vcc, -1, 0
	v_cndmask_b32_e32 v73, 0, v132, vcc
	v_add_u32_e32 v72, v72, v73
	s_cmp_gt_i32 s99, 13
	s_cselect_b64 vcc, -1, 0
	v_cndmask_b32_e32 v73, 0, v133, vcc
	v_add_u32_e32 v72, v72, v73
	s_cmp_gt_i32 s99, 14
	s_cselect_b64 vcc, -1, 0
	v_cndmask_b32_e32 v73, 0, v134, vcc
	v_add_u32_e32 v72, v72, v73
	s_cmp_gt_i32 s99, 15
	s_cselect_b64 vcc, -1, 0
	v_cndmask_b32_e32 v73, 0, v135, vcc
	v_add_u32_e32 v72, v72, v73
	s_cmp_gt_i32 s99, 16
	s_cselect_b64 vcc, -1, 0
	v_cndmask_b32_e32 v73, 0, v136, vcc
	v_add_u32_e32 v72, v72, v73
	s_cmp_gt_i32 s99, 17
	s_cselect_b64 vcc, -1, 0
	v_cndmask_b32_e32 v73, 0, v137, vcc
	v_add_u32_e32 v72, v72, v73
	s_cmp_gt_i32 s99, 18
	s_cselect_b64 vcc, -1, 0
	v_cndmask_b32_e32 v73, 0, v138, vcc
	v_add_u32_e32 v72, v72, v73
	s_cmp_gt_i32 s99, 19
	s_cselect_b64 vcc, -1, 0
	v_cndmask_b32_e32 v73, 0, v139, vcc
	v_add_u32_e32 v72, v72, v73
	s_cmp_gt_i32 s99, 20
	s_cselect_b64 vcc, -1, 0
	v_cndmask_b32_e32 v73, 0, v140, vcc
	v_add_u32_e32 v72, v72, v73
	s_cmp_gt_i32 s99, 21
	s_cselect_b64 vcc, -1, 0
	v_cndmask_b32_e32 v73, 0, v141, vcc
	v_add_u32_e32 v72, v72, v73
	s_cmp_gt_i32 s99, 22
	s_cselect_b64 vcc, -1, 0
	v_cndmask_b32_e32 v73, 0, v142, vcc
	v_add_u32_e32 v72, v72, v73
	s_cmp_gt_i32 s99, 23
	s_cselect_b64 vcc, -1, 0
	v_cndmask_b32_e32 v73, 0, v143, vcc
	v_add_u32_e32 v72, v72, v73
	s_cmp_gt_i32 s99, 24
	s_cselect_b64 vcc, -1, 0
	v_cndmask_b32_e32 v73, 0, v144, vcc
	v_add_u32_e32 v72, v72, v73
	s_cmp_gt_i32 s99, 25
	s_cselect_b64 vcc, -1, 0
	v_cndmask_b32_e32 v73, 0, v145, vcc
	v_add_u32_e32 v72, v72, v73
	s_cmp_gt_i32 s99, 26
	s_cselect_b64 vcc, -1, 0
	v_cndmask_b32_e32 v73, 0, v146, vcc
	v_add_u32_e32 v72, v72, v73
	s_cmp_gt_i32 s99, 27
	s_cselect_b64 vcc, -1, 0
	v_cndmask_b32_e32 v73, 0, v147, vcc
	v_add_u32_e32 v72, v72, v73
	s_cmp_gt_i32 s99, 28
	s_cselect_b64 vcc, -1, 0
	v_cndmask_b32_e32 v73, 0, v148, vcc
	v_add_u32_e32 v72, v72, v73
	s_cmp_gt_i32 s99, 29
	s_cselect_b64 vcc, -1, 0
	v_cndmask_b32_e32 v73, 0, v149, vcc
	v_add_u32_e32 v72, v72, v73
	s_cmp_gt_i32 s99, 30
	s_cselect_b64 vcc, -1, 0
	v_cndmask_b32_e32 v73, 0, v150, vcc
	v_add_u32_e32 v72, v72, v73
	s_cmp_gt_i32 s99, 31
	s_cselect_b64 vcc, -1, 0
	v_cndmask_b32_e32 v73, 0, v151, vcc
	v_add_u32_e32 v72, v72, v73
	v_add_u32_e32 v73, s51, v80
	ds_write2st64_b32 v73, v3, v72 offset1:8
	s_and_saveexec_b64 s[0:1], s[4:5]
	s_cbranch_execz .LBB0_1396
	s_mul_i32 s20, s2, 0x110
	v_add_u32_e32 v72, s20, v0
	v_ashrrev_i32_e32 v73, 31, v72
	v_lshl_add_u64 v[72:73], v[72:73], 2, s[48:49]
	global_load_dword v3, v[72:73], off
	s_waitcnt vmcnt(0)
	ds_write_b32 v81, v3 offset:4352

; __device__ __forceinline__ void phase_scatter(const Frame& F, int layer) {
;     ...
;     for (int vb = F.bid; vb < 256; vb += F.G) {
;         int all = 0, lo = 0;
;         for (int b = F.wave * 32; b < F.wave * 32 + 32; ++b) { const int h = HIST[b * 64 + F.lane]; all += h; lo += (b < vb) ? h : 0; }
;         pall[F.wave * 64 + F.lane] = all; plo[F.wave * 64 + F.lane] = lo;
;         const int rb = tok0 + vb * TPB;
;         for (int i = F.tid; i < TPB * 8; i += NTHREADS) sel_l[i] = SE[rb * 8 + i];
.LBB0_3140:
	s_lshl_b32 s33, s2, 5
	s_add_i32 s50, s33, 0x200
	global_load_dword v120, v[6:7], off
	global_load_dword v121, v[8:9], off
	global_load_dword v122, v[10:11], off
	global_load_dword v123, v[12:13], off
	global_load_dword v124, v[14:15], off
	global_load_dword v125, v[16:17], off
	global_load_dword v126, v[18:19], off
	global_load_dword v127, v[20:21], off
	global_load_dword v128, v[22:23], off
	global_load_dword v129, v[24:25], off
	global_load_dword v130, v[26:27], off
	global_load_dword v131, v[28:29], off
	global_load_dword v132, v[30:31], off
	global_load_dword v133, v[32:33], off
	global_load_dword v134, v[34:35], off
	global_load_dword v135, v[36:37], off
	global_load_dword v136, v[38:39], off
	global_load_dword v137, v[40:41], off
	global_load_dword v138, v[42:43], off
	global_load_dword v139, v[44:45], off
	global_load_dword v140, v[46:47], off
	global_load_dword v141, v[48:49], off
	global_load_dword v142, v[50:51], off
	global_load_dword v143, v[52:53], off
	global_load_dword v144, v[54:55], off
	global_load_dword v145, v[56:57], off
	global_load_dword v146, v[58:59], off
	global_load_dword v147, v[60:61], off
	global_load_dword v148, v[62:63], off
	global_load_dword v149, v[64:65], off
	global_load_dword v150, v[66:67], off
	global_load_dword v151, v[68:69], off
	s_sub_i32 s99, s2, s72
	v_mov_b32_e32 v72, 0
	s_waitcnt vmcnt(0)
	v_add_u32_e32 v3, v120, v121
	v_add3_u32 v3, v3, v122, v123
	v_add3_u32 v3, v3, v124, v125
	v_add3_u32 v3, v3, v126, v127
	v_add3_u32 v3, v3, v128, v129
	v_add3_u32 v3, v3, v130, v131
	v_add3_u32 v3, v3, v132, v133
	v_add3_u32 v3, v3, v134, v135
	v_add3_u32 v3, v3, v136, v137
	v_add3_u32 v3, v3, v138, v139
	v_add3_u32 v3, v3, v140, v141
	v_add3_u32 v3, v3, v142, v143
	v_add3_u32 v3, v3, v144, v145
	v_add3_u32 v3, v3, v146, v147
	v_add3_u32 v3, v3, v148, v149
	v_add3_u32 v3, v3, v150, v151
	s_cmp_gt_i32 s99, 0
	s_cselect_b64 vcc, -1, 0
	v_cndmask_b32_e32 v73, 0, v120, vcc
	v_add_u32_e32 v72, v72, v73
	s_cmp_gt_i32 s99, 1
	s_cselect_b64 vcc, -1, 0
	v_cndmask_b32_e32 v73, 0, v121, vcc
	v_add_u32_e32 v72, v72, v73
	s_cmp_gt_i32 s99, 2
	s_cselect_b64 vcc, -1, 0
	v_cndmask_b32_e32 v73, 0, v122, vcc
	v_add_u32_e32 v72, v72, v73
	s_cmp_gt_i32 s99, 3
	s_cselect_b64 vcc, -1, 0
	v_cndmask_b32_e32 v73, 0, v123, vcc
	v_add_u32_e32 v72, v72, v73
	s_cmp_gt_i32 s99, 4
	s_cselect_b64 vcc, -1, 0
	v_cndmask_b32_e32 v73, 0, v124, vcc
	v_add_u32_e32 v72, v72, v73
	s_cmp_gt_i32 s99, 5
	s_cselect_b64 vcc, -1, 0
	v_cndmask_b32_e32 v73, 0, v125, vcc
	v_add_u32_e32 v72, v72, v73
	s_cmp_gt_i32 s99, 6
	s_cselect_b64 vcc, -1, 0
	v_cndmask_b32_e32 v73, 0, v126, vcc
	v_add_u32_e32 v72, v72, v73
	s_cmp_gt_i32 s99, 7
	s_cselect_b64 vcc, -1, 0
	v_cndmask_b32_e32 v73, 0, v127, vcc
	v_add_u32_e32 v72, v72, v73
	s_cmp_gt_i32 s99, 8
	s_cselect_b64 vcc, -1, 0
	v_cndmask_b32_e32 v73, 0, v128, vcc
	v_add_u32_e32 v72, v72, v73
	s_cmp_gt_i32 s99, 9
	s_cselect_b64 vcc, -1, 0
	v_cndmask_b32_e32 v73, 0, v129, vcc
	v_add_u32_e32 v72, v72, v73
	s_cmp_gt_i32 s99, 10
	s_cselect_b64 vcc, -1, 0
	v_cndmask_b32_e32 v73, 0, v130, vcc
	v_add_u32_e32 v72, v72, v73
	s_cmp_gt_i32 s99, 11
	s_cselect_b64 vcc, -1, 0
	v_cndmask_b32_e32 v73, 0, v131, vcc
	v_add_u32_e32 v72, v72, v73
	s_cmp_gt_i32 s99, 12
	s_cselect_b64 vcc, -1, 0
	v_cndmask_b32_e32 v73, 0, v132, vcc
	v_add_u32_e32 v72, v72, v73
	s_cmp_gt_i32 s99, 13
	s_cselect_b64 vcc, -1, 0
	v_cndmask_b32_e32 v73, 0, v133, vcc
	v_add_u32_e32 v72, v72, v73
	s_cmp_gt_i32 s99, 14
	s_cselect_b64 vcc, -1, 0
	v_cndmask_b32_e32 v73, 0, v134, vcc
	v_add_u32_e32 v72, v72, v73
	s_cmp_gt_i32 s99, 15
	s_cselect_b64 vcc, -1, 0
	v_cndmask_b32_e32 v73, 0, v135, vcc
	v_add_u32_e32 v72, v72, v73
	s_cmp_gt_i32 s99, 16
	s_cselect_b64 vcc, -1, 0
	v_cndmask_b32_e32 v73, 0, v136, vcc
	v_add_u32_e32 v72, v72, v73
	s_cmp_gt_i32 s99, 17
	s_cselect_b64 vcc, -1, 0
	v_cndmask_b32_e32 v73, 0, v137, vcc
	v_add_u32_e32 v72, v72, v73
	s_cmp_gt_i32 s99, 18
	s_cselect_b64 vcc, -1, 0
	v_cndmask_b32_e32 v73, 0, v138, vcc
	v_add_u32_e32 v72, v72, v73
	s_cmp_gt_i32 s99, 19
	s_cselect_b64 vcc, -1, 0
	v_cndmask_b32_e32 v73, 0, v139, vcc
	v_add_u32_e32 v72, v72, v73
	s_cmp_gt_i32 s99, 20
	s_cselect_b64 vcc, -1, 0
	v_cndmask_b32_e32 v73, 0, v140, vcc
	v_add_u32_e32 v72, v72, v73
	s_cmp_gt_i32 s99, 21
	s_cselect_b64 vcc, -1, 0
	v_cndmask_b32_e32 v73, 0, v141, vcc
	v_add_u32_e32 v72, v72, v73
	s_cmp_gt_i32 s99, 22
	s_cselect_b64 vcc, -1, 0
	v_cndmask_b32_e32 v73, 0, v142, vcc
	v_add_u32_e32 v72, v72, v73
	s_cmp_gt_i32 s99, 23
	s_cselect_b64 vcc, -1, 0
	v_cndmask_b32_e32 v73, 0, v143, vcc
	v_add_u32_e32 v72, v72, v73
	s_cmp_gt_i32 s99, 24
	s_cselect_b64 vcc, -1, 0
	v_cndmask_b32_e32 v73, 0, v144, vcc
	v_add_u32_e32 v72, v72, v73
	s_cmp_gt_i32 s99, 25
	s_cselect_b64 vcc, -1, 0
	v_cndmask_b32_e32 v73, 0, v145, vcc
	v_add_u32_e32 v72, v72, v73
	s_cmp_gt_i32 s99, 26
	s_cselect_b64 vcc, -1, 0
	v_cndmask_b32_e32 v73, 0, v146, vcc
	v_add_u32_e32 v72, v72, v73
	s_cmp_gt_i32 s99, 27
	s_cselect_b64 vcc, -1, 0
	v_cndmask_b32_e32 v73, 0, v147, vcc
	v_add_u32_e32 v72, v72, v73
	s_cmp_gt_i32 s99, 28
	s_cselect_b64 vcc, -1, 0
	v_cndmask_b32_e32 v73, 0, v148, vcc
	v_add_u32_e32 v72, v72, v73
	s_cmp_gt_i32 s99, 29
	s_cselect_b64 vcc, -1, 0
	v_cndmask_b32_e32 v73, 0, v149, vcc
	v_add_u32_e32 v72, v72, v73
	s_cmp_gt_i32 s99, 30
	s_cselect_b64 vcc, -1, 0
	v_cndmask_b32_e32 v73, 0, v150, vcc
	v_add_u32_e32 v72, v72, v73
	s_cmp_gt_i32 s99, 31
	s_cselect_b64 vcc, -1, 0
	v_cndmask_b32_e32 v73, 0, v151, vcc
	v_add_u32_e32 v72, v72, v73
	v_add_u32_e32 v73, s51, v80
	ds_write2st64_b32 v73, v3, v72 offset1:8
	s_and_saveexec_b64 s[0:1], s[4:5]
	s_cbranch_execz .LBB0_3142
	v_lshl_or_b32 v72, s50, 3, v0
	v_ashrrev_i32_e32 v73, 31, v72
	v_lshl_add_u64 v[72:73], v[72:73], 2, s[48:49]
	global_load_dword v3, v[72:73], off
	s_waitcnt vmcnt(0)
	ds_write_b32 v81, v3 offset:4352
